# v66 + 3584 gate/up weight-conversion items of layer 1 moved from layer 0's in-projection tail into layer 1's own in-projection phase (upper half of the grid, idle for one unit there); layer-0 split re
# speedup vs baseline: 1.0128x; 1.0033x over previous
; #define LAS __attribute__((address_space(3)))
; __device__ __forceinline__ int opaque_tid() { int t = threadIdx.x; asm volatile("" : "+v"(t)); return t; }
;     __device__ __forceinline__ bool next(int i, Unit& u) const {
;         const long L = (long)i * G + c; if (L >= nwg) return false;
;         int wgid = (int)L; { const int q = nwg / NXCD, r = nwg % NXCD, xcd = wgid % NXCD, off = wgid / NXCD; wgid = (xcd < r ? xcd * (q + 1) : r * (q + 1) + (xcd - r) * q) + off; }
;         const int nig = WGM * nN, gid = wgid / nig, fm = gid * WGM, gsz = (nM - fm) < WGM ? (nM - fm) : WGM;
;         u.pm = fm + ((wgid % nig) % gsz); u.pn = (wgid % nig) / gsz; u.e = 0; u.rows = 256;
;         u.a = A + (size_t)u.pm * tstepA; u.b = Bt + (size_t)u.pn * tstep; return true;
; __device__ __forceinline__ void pj_mfma(const Args& a, LAS unsigned char* lds, int layer) {
;     pg8::DenseOrder So; So.init(a.ws + WS_ACT, a.ws + WS_WIN + (size_t)layer * 3328 * D * 2, NTOK, 3328, D, gridDim.x, blockIdx.x);
;     LAS float* gl = (LAS float*)(lds + SEG_OFF + 256);
;     { const int t_ = opaque_tid(); if (t_ < 256) { const int w = t_ >> 6, i = t_ & 63; const float* gp_ = w == 0 ? a.in[I_QGF] : w == 1 ? a.in[I_KGF] : w == 2 ? a.in[I_QGD] : a.in[I_KGD]; gl[t_] = gp_[layer * 64 + i]; } }
;     __syncthreads();
;     EpiProj E{(bf16_t*)(a.ws + WS_PROJ), gl};
;     pg8::gemm_phase<EpiProj, pg8::DenseOrder>(lds, D, So, E);
;     if ((int)blockIdx.x >= (int)gridDim.x - 32) cumsum_unit(a, lds, blockIdx.x - (gridDim.x - 32));
;     if (layer + 1 < NL) { __syncthreads(); constexpr int I_SPLIT = 10240;
;         const int half = gridDim.x / 2; const bool upper = (int)blockIdx.x >= half;
;         p0_prep(a, lds, layer + 1, upper ? half : 0, upper ? (int)gridDim.x - half : half, upper ? 0 : I_SPLIT, upper ? I_SPLIT : (1 << 30)); }
.LBB0_101:
	s_or_b64 exec, exec, s[0:1]
	s_mov_b32 vcc_lo, 0
	s_nop 1
	v_writelane_b32 v254, vcc_lo, 60
	s_nop 1
	s_mov_b32 vcc_lo, 0
	s_nop 1
	v_writelane_b32 v254, vcc_lo, 62
	s_nop 1
	s_waitcnt lgkmcnt(0)
	s_barrier
	s_load_dwordx2 s[92:93], s[54:55], 0xa0
	s_load_dwordx16 s[12:27], s[54:55], 0x20
	s_load_dwordx4 s[0:3], s[54:55], 0x90
	s_movk_i32 s5, 0xd1
	s_mov_b32 s67, 0
	s_waitcnt vmcnt(0)
	v_mbcnt_lo_u32_b32 v1, -1, 0
	v_mbcnt_hi_u32_b32 v199, -1, v1
	s_waitcnt lgkmcnt(0)
	v_writelane_b32 v252, s0, 8
	v_and_b32_e32 v240, 64, v199
	s_mul_hi_u32 s85, s77, 0x600
	v_writelane_b32 v252, s1, 9
	v_writelane_b32 v252, s2, 10
	v_writelane_b32 v252, s3, 11
	s_add_u32 s0, s92, 0x100000
	s_addc_u32 s1, s93, 0
	v_writelane_b32 v252, s0, 12
	s_add_u32 s96, s92, 0xbc00000
	s_addc_u32 s97, s93, 0
	v_writelane_b32 v252, s1, 13
	s_lshl_b32 s0, s61, 3
	s_add_u32 s10, s92, 0x180000
	s_addc_u32 s11, s93, 0
	s_add_u32 s80, s92, 0x7c00000
	s_addc_u32 s81, s93, 0
	v_writelane_b32 v252, s0, 14
	s_add_u32 s0, s92, 0xfc00000
	s_addc_u32 s1, s93, 0
	s_add_u32 s50, s92, 0x18c00000
	s_addc_u32 s51, s93, 0
	s_add_u32 s2, s92, 0xa00000
	s_addc_u32 s3, s93, 0
	v_writelane_b32 v252, s2, 15
	s_cmpk_lt_i32 s61, 0x680
	s_mul_i32 s84, s77, 0x600
	v_writelane_b32 v252, s3, 16
	s_cselect_b64 s[2:3], -1, 0
	v_writelane_b32 v252, s2, 17
	v_mov_b32_e32 v35, 0
	v_add_u32_e32 v241, 64, v240
	v_writelane_b32 v252, s3, 18
	s_ashr_i32 s2, s61, 31
	v_writelane_b32 v252, s2, 19
	s_lshr_b32 s2, s2, 29
	s_add_i32 s3, s61, s2
	s_ashr_i32 s2, s3, 3
	s_and_b32 s3, s3, -8
	s_sub_i32 s3, s61, s3
	s_lshl_b32 s4, s3, 6
	s_cmp_lt_i32 s3, 0
	s_cselect_b32 s5, s5, 0xd0
	s_mul_i32 s5, s5, s3
	s_mulk_i32 s3, 0x41
	s_cselect_b32 s3, s3, s4
	s_add_i32 s5, s5, s2
	s_mul_hi_i32 s4, s5, 0x4ec4ec4f
	s_lshr_b32 s6, s4, 31
	s_ashr_i32 s4, s4, 5
	s_add_i32 s4, s4, s6
	s_mul_i32 s6, s4, 0x68
	s_sub_i32 s5, s5, s6
	s_lshl_b32 s7, s4, 3
	s_bfe_i32 s4, s5, 0x80000
	s_bfe_u32 s4, s4, 0x3000c
	s_add_i32 s6, s5, s4
	s_bfe_i32 s4, s6, 0x80000
	s_and_b32 s6, s6, 0xf8
	s_sub_i32 s5, s5, s6
	s_sext_i32_i16 s8, s4
	s_sext_i32_i8 s5, s5
	s_add_i32 s28, s7, s5
	s_ashr_i32 s5, s8, 3
	v_writelane_b32 v252, s5, 20
	s_mov_b32 s6, s28
	s_ashr_i32 s29, s28, 31
	v_writelane_b32 v252, s6, 21
	s_lshr_b32 s4, s8, 3
	v_xor_b32_e32 v236, 16, v199
	v_writelane_b32 v252, s7, 22
	s_lshl_b64 s[6:7], s[28:29], 19
	s_add_u32 s6, s80, s6
	s_addc_u32 s7, s81, s7
	v_writelane_b32 v252, s6, 23
	s_bfe_i64 s[4:5], s[4:5], 0x100000
	s_lshl_b64 s[4:5], s[4:5], 19
	v_writelane_b32 v252, s7, 24
	v_writelane_b32 v252, s4, 25
	v_xor_b32_e32 v237, 32, v199
	v_mov_b32_e32 v238, 1
	v_writelane_b32 v252, s5, 26
	s_ashr_i32 s4, s77, 31
	v_writelane_b32 v252, s4, 27
	s_sub_i32 s4, s77, 32
	s_cmp_ge_i32 s61, s4
	s_cselect_b64 s[6:7], -1, 0
	v_writelane_b32 v252, s6, 28
	s_sub_i32 s4, s61, s4
	s_and_b32 s5, s4, 3
	v_writelane_b32 v252, s7, 29
	s_ashr_i32 s6, s4, 2
	s_ashr_i32 s7, s6, 31
	s_lshl_b32 s5, s5, 2
	s_add_u32 s5, s10, s5
	v_writelane_b32 v252, s10, 30
	s_addc_u32 s8, s11, 0
	s_lshl_b64 s[6:7], s[6:7], 16
	s_add_u32 s6, s5, s6
	s_addc_u32 s7, s8, s7
	s_add_u32 s28, s92, 0x200000
	s_addc_u32 s29, s93, 0
	s_ashr_i32 s5, s4, 31
	s_lshl_b64 s[4:5], s[4:5], 14
	v_writelane_b32 v252, s11, 31
	s_add_u32 s4, s28, s4
	v_writelane_b32 v252, s6, 32
	s_addc_u32 s5, s29, s5
	s_lshr_b32 s8, s77, 1
	v_writelane_b32 v252, s7, 33
	s_sub_i32 s9, s77, s8
	v_writelane_b32 v252, s4, 34
	s_cmp_lt_i32 s61, s8
	v_mov_b32_e32 v198, 0x358637bd
	v_writelane_b32 v252, s5, 35
	s_cselect_b64 s[4:5], -1, 0
	s_and_b64 s[6:7], s[4:5], exec
	s_cselect_b32 s6, s8, s9
	s_movk_i32 s7, 0x1a80
	s_cselect_b32 s10, 0, s8
	s_cselect_b32 s8, 0x16c8, 0
	s_cselect_b32 s7, s7, 0x16c8
	s_lshl_b32 s6, s6, 3
	v_writelane_b32 v252, s7, 36
	s_cmp_ge_i32 s61, s10
	v_writelane_b32 v252, s6, 37
	s_cselect_b64 s[6:7], -1, 0
	s_or_b64 s[4:5], s[36:37], s[4:5]
	s_load_dwordx8 s[36:43], s[54:55], 0x60
	s_and_b64 s[4:5], s[6:7], s[4:5]
	v_writelane_b32 v252, s4, 38
	v_mov_b32_e32 v201, 1.0
	v_mov_b32_e32 v239, 0x7f800000
	v_writelane_b32 v252, s5, 39
	s_sub_i32 s4, s61, s10
	s_lshl_b32 s4, s4, 3
	s_add_i32 s4, s4, s8
	s_waitcnt lgkmcnt(0)
	s_mov_b64 s[8:9], s[40:41]
	v_writelane_b32 v252, s4, 40
	s_add_u32 s6, s38, 0x400000
	s_mov_b64 s[10:11], s[42:43]
	s_mov_b64 s[4:5], s[36:37]
	v_writelane_b32 v252, s4, 41
	v_mov_b32_e32 v202, 0x3f317218
	v_mov_b32_e32 v242, 0xff800000
	v_writelane_b32 v252, s5, 42
	v_writelane_b32 v252, s6, 43
	v_writelane_b32 v252, s7, 44
	v_writelane_b32 v252, s8, 45
	v_writelane_b32 v252, s9, 46
	v_writelane_b32 v252, s10, 47
	v_writelane_b32 v252, s11, 48
	s_addc_u32 s7, s39, 0
	v_writelane_b32 v252, s6, 49
	s_add_u32 s4, s16, 0xd04000
	s_movk_i32 s74, 0x1ff
	v_writelane_b32 v252, s7, 50
	v_writelane_b32 v252, s12, 51
	s_addc_u32 s5, s17, 0
	s_mov_b32 s76, 0x800000
	v_writelane_b32 v255, s25, 0
	v_writelane_b32 v255, s26, 1
	v_writelane_b32 v255, s27, 2
	v_writelane_b32 v255, s4, 3
	v_writelane_b32 v252, s13, 52
	v_writelane_b32 v252, s14, 53
	v_writelane_b32 v255, s5, 4
	s_add_u32 s4, s92, 0x5b00000
	s_addc_u32 s5, s93, 0
	v_writelane_b32 v255, s4, 5
	v_writelane_b32 v252, s15, 54
	v_writelane_b32 v252, s16, 55
	v_writelane_b32 v255, s5, 6
	s_add_u32 s4, s92, 0x1b00000
	s_addc_u32 s5, s93, 0
	s_add_u32 s82, s92, 0x700000
	v_writelane_b32 v255, s4, 7
	s_addc_u32 s83, s93, 0
	v_writelane_b32 v252, s17, 56
	v_writelane_b32 v255, s5, 8
	s_add_u32 s4, s92, 0x14000
	v_writelane_b32 v255, s4, 9
	s_addc_u32 s4, s93, 0
	s_add_i32 s6, s61, 0x900
	s_cmpk_lt_i32 s61, 0x200
	v_writelane_b32 v255, s4, 10
	s_cselect_b64 s[4:5], -1, 0
	v_writelane_b32 v255, s4, 11
	v_writelane_b32 v252, s18, 57
;     ...
;         if (u < AT_NFOX) {
;             const int qb = 15 - (u >> 5), bh = u & 31, b = bh >> 2, h = bh & 3, q0 = qb * 256;
;             const size_t rb = (size_t)b * S;
;             const bf16_t* Kb = proj + ((size_t)(4 + h) * NTOK + rb) * 64;
;             const bf16_t* Vb = proj + ((size_t)(8 + h) * NTOK + rb) * 64;
;             const float* cum = cumall + (size_t)bh * S;
;             const int jhi = 4 * qb + 3;
;             fox_cr = cum[q0]; fox_cv = cum[64 * (lane <= jhi ? lane : jhi) + 63]; fox_cq = cum[q0 + 32 * wid + r32];
;             if (!(dbg & 1)) { FOX_ISSUE(0); FOX_ISSUE(1); FOX_ISSUE(2); }
;             const bf16_t* Q = proj + ((size_t)(0 + h) * NTOK + rb + q0 + 32 * wid + r32) * 64;
; #pragma unroll
;             for (int d0 = 0; d0 < 4; ++d0) qr[d0] = *(const bf16x8*)(Q + d0 * 16 + hi * 8);
;         } else if (u < AT_NFOX + AT_NDIL) {
;             const int v2 = u - AT_NFOX, bh = v2 % 48, rest = v2 / 48, b = bh / 6, h = bh % 6, p = rest >> 4, x = rest & 15;
;             const int dil = p == 0 ? 1 : p == 1 ? 4 : 16, res = x % dil, nb2 = x / dil;
;             const size_t rb = (size_t)b * S;
;             const bf16_t* Kb = proj + ((size_t)(22 + h) * NTOK + rb) * 64;
;             const bf16_t* Vb = proj + ((size_t)(28 + h) * NTOK + rb) * 64;
;             const int mk_base = 256 * nb2 - 128, tt_lo = nb2 == 0 ? 2 : 0;
;             const size_t rs = (size_t)64 * dil;
; #pragma unroll
;     ...
;             if (tid < 256) { const int st = tid - 64; tab[tid] = (st >= 0 && st <= 128) ? relb[t5_bucket(st * dil) * 6 + h] : -INFINITY; }
;             const size_t trow = (size_t)(256 * nb2 + 32 * wid + r32) * dil + res;
;             const bf16_t* Q = proj + ((size_t)(16 + h) * NTOK + rb + trow) * 64;
; #pragma unroll
;             for (int d0 = 0; d0 < 4; ++d0) qr[d0] = *(const bf16x8*)(Q + d0 * 16 + hi * 8);
;         } else {
;             const int v2 = u - AT_NFOX - AT_NDIL, qb = 15 - v2 / 48, bh = v2 % 48, b = bh / 6, h = bh % 6, q0 = qb * 256;
;             const size_t rb = (size_t)b * S;
;             const bf16_t* Kb = proj + ((size_t)(40 + h) * NTOK + rb) * 64;
;             const bf16_t* Vb = proj + ((size_t)(46 + h) * NTOK + rb) * 64;
;             const int jhi = (q0 + 254) >> 6;
;             if (!(dbg & 1)) { SB_ISSUE(0); SB_ISSUE(1); SB_ISSUE(2); }
	v_writelane_b32 v252, s19, 58
	v_writelane_b32 v255, s5, 12
	s_and_b64 s[4:5], s[4:5], exec
	s_cselect_b32 s13, s61, s6
	s_cmpk_lt_i32 s13, 0xe00
	s_cselect_b64 s[4:5], -1, 0
	v_writelane_b32 v255, s4, 13
	s_cmpk_gt_i32 s13, 0x1ff
	s_mov_b32 s17, s67
	v_writelane_b32 v255, s5, 14
	s_cselect_b64 s[4:5], -1, 0
	v_writelane_b32 v255, s4, 15
	s_cmpk_gt_u32 s13, 0xaff
	v_writelane_b32 v252, s20, 59
	v_writelane_b32 v255, s5, 16
	s_cselect_b64 s[4:5], -1, 0
	v_writelane_b32 v255, s4, 17
	v_writelane_b32 v252, s21, 60
	s_mov_b32 s21, s67
	v_writelane_b32 v255, s5, 18
	s_add_i32 s4, s13, 0xf500
	s_and_b32 s5, s4, 0xffff
	s_mul_i32 s5, s5, 0xaaab
	s_lshr_b32 s5, s5, 21
	s_mul_i32 s6, s5, 48
	s_sub_i32 s4, s4, s6
	s_and_b32 s6, s4, 0xff
	s_mulk_i32 s6, 0xab
	s_bfe_u32 s6, s6, 0x6000a
	s_mul_i32 s7, s6, 6
	s_sub_i32 s4, s4, s7
	s_and_b32 s4, s4, 0xff
	s_lshl_b32 s6, s6, 12
	s_lshl_b32 s4, s4, 15
	s_add_i32 s7, s6, s4
	s_lshl_b32 s7, s7, 7
	s_add_i32 s8, s7, 0xb800000
	s_add_u32 s8, s96, s8
	s_addc_u32 s9, s97, 0
	s_add_i32 s7, s7, 0xa000000
	s_add_u32 s7, s96, s7
	s_addc_u32 s10, s97, 0
	s_lshl_b32 s11, s5, 14
	s_sub_i32 s12, 0x3f000, s11
	s_lshl_b32 s12, s12, 1
	s_add_u32 s14, s7, s12
	s_addc_u32 s15, s10, 0
	v_writelane_b32 v255, s14, 19
	v_writelane_b32 v252, s22, 61
	v_writelane_b32 v252, s23, 62
	v_writelane_b32 v255, s15, 20
	s_add_u32 s14, s8, s12
	s_addc_u32 s15, s9, 0
	s_sub_i32 s12, 0x3e000, s11
	v_writelane_b32 v255, s14, 21
	s_lshl_b32 s12, s12, 1
	v_writelane_b32 v252, s24, 63
	v_writelane_b32 v255, s15, 22
	s_add_u32 s14, s7, s12
	s_addc_u32 s15, s10, 0
	v_writelane_b32 v255, s14, 23
	s_movk_i32 s56, 0x7f
	s_mov_b32 s57, 0xff800000
	v_writelane_b32 v255, s15, 24
	s_add_u32 s14, s8, s12
	s_addc_u32 s15, s9, 0
	s_sub_i32 s11, 0x3d000, s11
	v_writelane_b32 v255, s14, 25
	s_lshl_b32 s11, s11, 1
	s_mov_b32 s65, 0xc2ce8ed0
	v_writelane_b32 v255, s15, 26
	s_add_u32 s14, s7, s11
	s_addc_u32 s15, s10, 0
	s_add_u32 s8, s8, s11
	s_addc_u32 s9, s9, 0
	s_lshl_b32 s5, s5, 8
	s_sub_i32 s4, s4, s5
	s_add_i32 s5, s13, 0xfe00
	s_add_i32 s4, s4, s6
	s_and_b32 s6, s5, 0xffff
	s_mul_i32 s6, s6, 0xaaab
	s_lshr_b32 s7, s6, 21
	s_mul_i32 s7, s7, 48
	s_sub_i32 s5, s5, s7
	v_writelane_b32 v255, s14, 27
	s_and_b32 s7, s5, 0xff
	s_mulk_i32 s7, 0xab
	v_writelane_b32 v255, s15, 28
	v_writelane_b32 v255, s8, 29
	s_bfe_u32 s7, s7, 0x6000a
	s_add_i32 s4, s4, 0x110f00
	v_writelane_b32 v255, s9, 30
	s_mul_i32 s8, s7, 6
	s_sub_i32 s5, s5, s8
	s_and_b32 s5, s5, 0xff
	s_lshl_b32 s7, s7, 12
	s_lshl_b32 s8, s5, 15
	s_add_i32 s7, s7, s8
	v_writelane_b32 v255, s4, 31
	s_bfe_u32 s4, s6, 0x40015
	s_lshl_b32 s6, s7, 7
	s_add_u32 s6, s96, s6
	s_addc_u32 s8, s97, 0
	s_add_u32 s9, s6, 0x5800000
	s_addc_u32 s10, s8, 0
	s_add_u32 s6, s6, 0x7000000
	s_addc_u32 s8, s8, 0
	s_lshl_b32 s11, s4, 7
	s_or_b32 s12, s11, 0x60000
	s_add_u32 s14, s9, s12
	s_addc_u32 s15, s10, 0
	v_writelane_b32 v255, s14, 32
	s_mov_b64 s[44:45], -1
	s_mov_b64 s[86:87], 0x800
	v_writelane_b32 v255, s15, 33
	s_add_u32 s14, s6, s12
	s_addc_u32 s15, s8, 0
	v_writelane_b32 v255, s14, 34
	s_or_b32 s12, s11, 0x40000
	s_mov_b32 s60, 0xbfb8aa3b
	v_writelane_b32 v255, s15, 35
	s_add_u32 s14, s9, s12
	s_addc_u32 s15, s10, 0
	v_writelane_b32 v255, s14, 36
	s_mov_b64 s[88:89], 0x80
	s_mov_b64 s[94:95], 0x100
	v_writelane_b32 v255, s15, 37
	s_add_u32 s14, s6, s12
	s_addc_u32 s15, s8, 0
	v_writelane_b32 v255, s14, 38
	s_or_b32 s12, s11, 0x20000
	s_mov_b32 s62, s67
	v_writelane_b32 v255, s15, 39
	s_add_u32 s14, s9, s12
	s_addc_u32 s15, s10, 0
	v_writelane_b32 v255, s14, 40
	s_nop 1
	v_writelane_b32 v255, s15, 41
	s_add_u32 s14, s6, s12
	s_addc_u32 s15, s8, 0
	v_writelane_b32 v255, s14, 42
	s_nop 1
	v_writelane_b32 v255, s15, 43
	s_add_u32 s14, s9, s11
	s_addc_u32 s15, s10, 0
	v_writelane_b32 v255, s14, 44
	s_add_u32 s10, s6, s11
	s_addc_u32 s11, s8, 0
	v_writelane_b32 v255, s15, 45
	s_lshl_b32 s5, s5, 2
	v_writelane_b32 v255, s10, 46
	s_add_i32 s5, s5, 0
	s_add_i32 s5, s5, 0x21f00
	v_writelane_b32 v255, s11, 47
	v_writelane_b32 v255, s5, 48
	s_ashr_i32 s5, s13, 5
	s_or_b32 s4, s7, s4
	s_sub_i32 s5, 15, s5
	s_lshl_b32 s6, s13, 10
	s_and_b32 s7, s13, 31
	s_and_b32 s6, s6, 0x7000
	s_lshl_b32 s7, s7, 14
	s_or_b32 s14, s4, 0x80000
	s_and_b32 s8, s13, 3
	s_lshl_b32 s16, s5, 8
	s_add_u32 s18, s28, s7
	s_addc_u32 s19, s29, 0
	s_lshl_b32 s7, s5, 2
	v_writelane_b32 v255, s13, 49
	s_or_b32 s20, s7, 3
	s_lshl_b64 s[4:5], s[16:17], 2
	v_writelane_b32 v255, s28, 50
	s_add_u32 s4, s18, s4
	v_writelane_b32 v255, s29, 51
	s_addc_u32 s5, s19, s5
	v_writelane_b32 v255, s4, 52
	s_mov_b32 s15, s67
	s_nop 0
	v_writelane_b32 v255, s5, 53
	s_lshl_b32 s4, s8, 22
	s_lshl_b32 s5, s6, 7
	s_or_b32 s4, s5, s4
	s_add_u32 s4, s96, s4
	s_addc_u32 s5, s97, 0
	s_add_u32 s9, s4, 0x2000000
	s_addc_u32 s10, s5, 0
	s_add_u32 s11, s4, 0x1000000
	s_addc_u32 s12, s5, 0
	s_lshl_b64 s[4:5], s[20:21], 13
	s_add_u32 s22, s11, s4
	s_addc_u32 s23, s12, s5
	v_writelane_b32 v255, s22, 54
	s_add_u32 s4, s9, s4
	s_addc_u32 s5, s10, s5
	v_writelane_b32 v255, s23, 55
	v_writelane_b32 v255, s4, 56
	s_lshl_b32 s66, s20, 6
	s_nop 0
	v_writelane_b32 v255, s5, 57
	s_mov_b32 s4, s20
	v_writelane_b32 v255, s4, 58
	s_nop 1
	v_writelane_b32 v255, s5, 59
	s_lshl_b64 s[4:5], s[66:67], 2
	s_add_u32 s4, s18, s4
	s_addc_u32 s5, s19, s5
; #define LAS __attribute__((address_space(3)))
; #define FOX_ISSUE(i) do { const int j_ = jhi - (i), bf_ = (i) & 3; dma_kv(lds, bf_, Kb + (size_t)j_ * 4096, Vb + (size_t)j_ * 4096, 64, wid, lane); \
;         glds4(cum + j_ * 64 + lane, (unsigned)__builtin_amdgcn_readfirstlane(l0 + L_CK + bf_ * 256)); } while (0)
;     ...
;     bf16x8 qr[4];
;     float fox_cr = 0.f, fox_cv = 0.f, fox_cq = 0.f;
;     auto prologue = [&](int u) {
;         if (!UNIT_ON(u)) return;
;         int lane = tid & 63; asm volatile("" : "+v"(lane));
;         const int r32 = lane & 31, hi = lane >> 5;
;         if (u < AT_NFOX) {
;             const int qb = 15 - (u >> 5), bh = u & 31, b = bh >> 2, h = bh & 3, q0 = qb * 256;
;             const size_t rb = (size_t)b * S;
;             const bf16_t* Kb = proj + ((size_t)(4 + h) * NTOK + rb) * 64;
;             const bf16_t* Vb = proj + ((size_t)(8 + h) * NTOK + rb) * 64;
;             const float* cum = cumall + (size_t)bh * S;
;             const int jhi = 4 * qb + 3;
;             fox_cr = cum[q0]; fox_cv = cum[64 * (lane <= jhi ? lane : jhi) + 63]; fox_cq = cum[q0 + 32 * wid + r32];
;             if (!(dbg & 1)) { FOX_ISSUE(0); FOX_ISSUE(1); FOX_ISSUE(2); }
;             const bf16_t* Q = proj + ((size_t)(0 + h) * NTOK + rb + q0 + 32 * wid + r32) * 64;
; #pragma unroll
;             for (int d0 = 0; d0 < 4; ++d0) qr[d0] = *(const bf16x8*)(Q + d0 * 16 + hi * 8);
; __device__ __forceinline__ void op_mfma(const Args& a, LAS unsigned char* lds, int layer, bf16_t* outp = nullptr) {
;     pg8::DenseOrder So; So.init(a.ws + WS_ACT, a.ws + WS_WOUT + (size_t)layer * D * D * 2, NTOK, D, D, gridDim.x, blockIdx.x, (size_t)256 * 128);
;     bf16_t* xb = (bf16_t*)(a.ws + WS_XB);
;     EpiOut E{layer == 0 ? a.in[I_X] : nullptr, xb, outp ? outp : xb, (const float*)(a.ws + WS_MOD) + (size_t)layer * NB * 6144 + 2048};
;     pg8::gemm_phase<EpiOut, pg8::DenseOrder>(lds, D, So, E, 128u, (size_t)NTOK * 128);
	v_writelane_b32 v255, s4, 60
	s_or_b32 s66, s7, 2
	s_nop 0
	v_writelane_b32 v255, s5, 61
	s_lshl_b64 s[4:5], s[66:67], 13
	s_add_u32 s20, s11, s4
	s_addc_u32 s21, s12, s5
	s_add_u32 s4, s9, s4
	s_addc_u32 s5, s10, s5
	v_writelane_b32 v253, s4, 0
	s_lshl_b32 s66, s66, 6
	v_writelane_b32 v255, s20, 62
	v_writelane_b32 v253, s5, 1
	s_lshl_b64 s[4:5], s[66:67], 2
	s_add_u32 s4, s18, s4
	s_addc_u32 s5, s19, s5
	v_writelane_b32 v253, s4, 2
	s_or_b32 s66, s7, 1
	v_writelane_b32 v255, s21, 63
	v_writelane_b32 v253, s5, 3
	s_lshl_b64 s[4:5], s[66:67], 13
	s_add_u32 s20, s11, s4
	s_addc_u32 s21, s12, s5
	v_writelane_b32 v253, s20, 4
	s_add_u32 s4, s9, s4
	s_addc_u32 s5, s10, s5
	v_writelane_b32 v253, s21, 5
	v_writelane_b32 v253, s4, 6
	s_lshl_b32 s66, s66, 6
	s_mov_b32 s9, s67
	v_writelane_b32 v253, s5, 7
	s_lshl_b64 s[4:5], s[66:67], 2
	s_add_u32 s4, s18, s4
	v_writelane_b32 v253, s18, 8
	s_addc_u32 s5, s19, s5
	s_nop 0
	v_writelane_b32 v253, s19, 9
	v_writelane_b32 v253, s4, 10
	s_nop 1
	v_writelane_b32 v253, s5, 11
	s_lshl_b32 s4, s8, 15
	s_or_b32 s4, s6, s4
	s_mov_b32 s6, s16
	v_writelane_b32 v253, s6, 12
	s_add_i32 s4, s4, s16
	s_mov_b32 s8, s77
	v_writelane_b32 v253, s7, 13
	s_mov_b32 s6, s61
	s_mov_b32 s7, s67
	v_writelane_b32 v253, s4, 14
	s_lshl_b64 s[4:5], s[6:7], 9
	s_lshl_b64 s[70:71], s[8:9], 9
	v_writelane_b32 v253, s4, 15
	s_nop 1
	v_writelane_b32 v253, s5, 16
	s_add_u32 s4, s92, 0x8c00000
	s_addc_u32 s5, s93, 0
	v_writelane_b32 v253, s4, 17
	s_nop 1
	v_writelane_b32 v253, s5, 18
	s_add_u32 s4, s92, 0x1700000
	v_writelane_b32 v253, s4, 19
	s_addc_u32 s4, s93, 0
	v_writelane_b32 v253, s4, 20
	s_add_u32 s4, s92, 0x10000
	v_writelane_b32 v253, s4, 21
	s_addc_u32 s4, s93, 0
	v_writelane_b32 v253, s4, 22
	s_add_u32 s4, s92, 0x300000
	s_addc_u32 s5, s93, 0
	v_writelane_b32 v253, s4, 23
	s_nop 1
	v_writelane_b32 v253, s5, 24
	s_add_u32 s4, s92, 0x500000
	s_addc_u32 s5, s93, 0
	v_writelane_b32 v253, s4, 25
	s_cmpk_lt_i32 s61, 0x100
	s_nop 0
	v_writelane_b32 v253, s5, 26
	s_cselect_b64 s[4:5], -1, 0
	v_writelane_b32 v253, s4, 27
	s_nop 1
	v_writelane_b32 v253, s5, 28
	s_add_u32 s4, s92, 0x14400000
	s_addc_u32 s5, s93, 0
	v_writelane_b32 v253, s4, 29
	s_nop 1
	v_writelane_b32 v253, s5, 30
	s_add_i32 s4, s77, s61
	v_writelane_b32 v253, s4, 31
	s_add_u32 s4, s92, 0x7c00080
	s_addc_u32 s5, s93, 0
	s_add_i32 s2, s3, s2
	s_ashr_i32 s3, s2, 31
	s_lshr_b32 s3, s3, 27
	v_writelane_b32 v253, s4, 32
	s_add_i32 s3, s2, s3
	s_nop 0
	v_writelane_b32 v253, s5, 33
	s_and_b32 s4, s3, 0xffe0
	s_sub_i32 s2, s2, s4
	s_bfe_i32 s4, s2, 0x80000
	s_bfe_u32 s4, s4, 0x3000c
	s_add_i32 s4, s2, s4
	s_and_b32 s5, s4, 0xf8
	s_sub_i32 s2, s2, s5
	s_ashr_i32 s3, s3, 5
	s_bfe_i32 s4, s4, 0x80000
	s_lshl_b32 s3, s3, 3
	s_sext_i32_i16 s4, s4
	s_sext_i32_i8 s2, s2
	s_add_i32 s10, s3, s2
	s_ashr_i32 s2, s4, 3
	v_writelane_b32 v253, s2, 34
	s_lshr_b32 s2, s4, 3
	s_mov_b32 s4, s10
	s_ashr_i32 s11, s10, 31
	v_writelane_b32 v253, s4, 35
	s_nop 1
	v_writelane_b32 v253, s5, 36
	s_lshl_b64 s[4:5], s[10:11], 15
	s_add_u32 s4, s80, s4
	s_addc_u32 s5, s81, s5
	v_writelane_b32 v253, s14, 37
	s_bfe_i64 s[2:3], s[2:3], 0x100000
	s_lshl_b64 s[2:3], s[2:3], 19
	v_writelane_b32 v253, s15, 38
	v_writelane_b32 v253, s2, 39
	s_nop 1
	v_writelane_b32 v253, s3, 40
	s_add_u32 s2, s4, 0x4000
	s_addc_u32 s3, s5, 0
	v_writelane_b32 v253, s2, 41
	s_nop 1
	v_writelane_b32 v253, s3, 42
	s_add_u32 s2, s4, 0x400000
	v_writelane_b32 v253, s4, 43
	s_addc_u32 s3, s5, 0
	s_lshl_b64 s[52:53], s[8:9], 10
	v_writelane_b32 v253, s5, 44
	v_writelane_b32 v253, s2, 45
	s_add_i32 s64, 0, 0x13000
	s_nop 0
	v_writelane_b32 v253, s3, 46
	s_lshl_b32 s2, s61, 7
	v_writelane_b32 v253, s2, 47
	s_lshl_b32 s2, s77, 7
	v_writelane_b32 v253, s2, 48
	s_mul_i32 s2, s77, 0x3000
	v_writelane_b32 v253, s2, 49
	s_add_i32 s2, 0, 0x21c20
	v_writelane_b32 v253, s2, 50
	s_add_i32 s2, 0, 0x21c24
	v_writelane_b32 v253, s2, 51
	s_add_i32 s2, 0, 0x21000
	v_writelane_b32 v253, s2, 52
	s_add_i32 s2, 0, 0x21100
	v_writelane_b32 v253, s2, 53
	s_add_i32 s2, 0, 0x21200
	v_writelane_b32 v253, s2, 54
	s_add_i32 s2, 0, 0x21504
	v_writelane_b32 v253, s2, 55
	s_add_i32 s2, 0, 0x15040
	v_writelane_b32 v253, s2, 56
	s_add_i32 s2, 0, 0x15000
	v_writelane_b32 v253, s2, 57
	s_add_i32 s2, 0, 0x21e80
	v_writelane_b32 v253, s2, 58
	s_add_i32 s2, 0, 0x21e10
	v_writelane_b32 v253, s2, 59
	s_add_i32 s2, 0, 0x21e20
	v_writelane_b32 v253, s2, 60
	s_add_i32 s2, 0, 0x21e30
	v_writelane_b32 v253, s2, 61
	v_writelane_b32 v253, s54, 62
	s_load_dwordx2 s[4:5], s[54:55], 0x0
	s_mov_b32 s3, 0x42b17218
	v_writelane_b32 v253, s55, 63
	s_waitcnt lgkmcnt(0)
	v_writelane_b32 v254, s4, 0
	s_nop 1
	v_writelane_b32 v254, s5, 1
	s_lshl_b64 s[4:5], s[8:9], 13
	v_writelane_b32 v254, s4, 2
	s_nop 1
	v_writelane_b32 v254, s5, 3
	v_writelane_b32 v254, s6, 4
	s_lshl_b64 s[4:5], s[6:7], 12
	s_nop 0
	v_writelane_b32 v254, s7, 5
	v_writelane_b32 v254, s4, 6
	s_nop 1
	v_writelane_b32 v254, s5, 7
	s_lshl_b64 s[4:5], s[8:9], 14
	v_writelane_b32 v254, s4, 8
	s_nop 1
	v_writelane_b32 v254, s5, 9
	v_writelane_b32 v254, s8, 10
	s_lshl_b64 s[4:5], s[8:9], 12
	s_nop 0
	v_writelane_b32 v254, s9, 11
	v_writelane_b32 v254, s4, 12
	s_nop 1
	v_writelane_b32 v254, s5, 13
	v_writelane_b32 v254, s82, 14
	s_nop 1
	v_writelane_b32 v254, s83, 15
	s_branch .LBB0_104

; __device__ __forceinline__ PrepItem prep_decode(const Args& a, int l, int r) {
;     constexpr int I_IN = 16 * 104, I_OUT = 16 * 32, I_GU = 16 * 16 * 32;
;     PrepItem p;
;     if (r < I_IN) {
;         const int kb = r / 104, nb = r % 104, cp = nb * 32;
;         const int lc = slot_col(4 * (cp >> 8) + ((cp >> 5) & 3)) + 32 * ((cp >> 7) & 1);
;         p.src = a.in[I_WIN] + (size_t)l * D * IN_COLS + (size_t)kb * 64 * IN_COLS + lc; p.ldw = IN_COLS;
;         p.dst = (bf16_t*)(a.ws + WS_WIN) + ((size_t)l * 3328 + cp) * D + kb * 64; p.K = D; return p;
;     }
;     r -= I_IN;
;     if (r < I_OUT) {
;         const int kb = r / 32, nb = r % 32;
;         p.src = a.in[I_WOUT] + (size_t)l * D * D + (size_t)kb * 64 * D + nb * 32; p.ldw = D;
;         p.dst = (bf16_t*)(a.ws + WS_WOUT) + ((size_t)l * D + nb * 32) * D + kb * 64; p.K = D; return p;
;     }
;     r -= I_OUT;
;     if (r < I_GU) {
;         const int e = r / 512, r2 = r % 512, kb = r2 / 32, nb = r2 % 32, pn = nb >> 3, bj = (nb >> 2) & 1, sub = nb & 3;
;         p.src = a.in[bj ? I_WU : I_WG] + ((size_t)l * NE + e) * D * DFF + (size_t)kb * 64 * DFF + 128 * pn + 32 * sub; p.ldw = DFF;
;         p.dst = (bf16_t*)(a.ws + WS_WGU) + (((size_t)l * NE + e) * 1024 + nb * 32) * D + kb * 64; p.K = D; return p;
;     }
;     r -= I_GU;
;     { const int e = r / 256, r2 = r % 256, kb = r2 / 32, nb = r2 % 32;
;       p.src = a.in[I_WD] + ((size_t)l * NE + e) * DFF * D + (size_t)kb * 64 * D + nb * 32; p.ldw = D;
;       p.dst = (bf16_t*)(a.ws + WS_WDN) + (((size_t)l * NE + e) * 1024 + nb * 32) * DFF + kb * 64; p.K = DFF; return p; }
;     ...
;     const int gw = ((int)blockIdx.x - blk0) * NWAVES + wave, ngw = nblk * NWAVES;
;     constexpr int I_L = 16 * 104 + 16 * 32 + 16 * 16 * 32 + 16 * 8 * 32;
;     if ((int)blockIdx.x < blk0 || (int)blockIdx.x >= blk0 + nblk) return;
;     float tv[32];
;     const int I_E = it_hi < I_L ? it_hi : I_L;
;     int it = it_lo + gw;
;     if (it < I_E) { const PrepItem p = prep_decode(a, l, it);
; #pragma unroll
;         for (int i = 0; i < 32; ++i) tv[i] = __builtin_nontemporal_load(p.src + (size_t)(2 * i + (lane >> 5)) * p.ldw + (lane & 31)); }
.Lprep_go:
	v_readlane_b32 s4, v252, 38
	v_readlane_b32 s5, v252, 39
	v_mov_b32_e32 v42, v0
	s_andn2_b64 vcc, exec, s[4:5]
	s_waitcnt vmcnt(0)
	s_barrier
	s_cbranch_vccnz .LBB0_346
	v_ashrrev_i32_e32 v1, 6, v42
	v_readlane_b32 s2, v252, 40
	s_nop 1
	v_add_u32_e32 v37, s2, v1
	v_readlane_b32 s2, v252, 36
	s_nop 1
	v_cmp_gt_i32_e32 vcc, s2, v37
	s_and_saveexec_b64 s[6:7], vcc
	s_cbranch_execz .LBB0_345
	s_movk_i32 s2, 0x67f
	v_cmp_lt_i32_e32 vcc, s2, v37
	s_and_saveexec_b64 s[4:5], vcc
	s_xor_b64 s[4:5], exec, s[4:5]
	s_cbranch_execz .LBB0_315
	s_movk_i32 s2, 0x87f
	v_cmp_lt_u32_e32 vcc, s2, v37
	s_and_saveexec_b64 s[8:9], vcc
	s_xor_b64 s[8:9], exec, s[8:9]
	s_cbranch_execz .LBB0_312
	s_movk_i32 s2, 0x287f
	v_cmp_lt_u32_e32 vcc, s2, v37
	s_and_saveexec_b64 s[10:11], vcc
	s_xor_b64 s[10:11], exec, s[10:11]
	s_cbranch_execz .LBB0_309
	v_add_u32_e32 v4, 0xffffd780, v37
	v_lshrrev_b32_e32 v2, 8, v4
	v_add_u32_e32 v34, 16, v2
	v_readlane_b32 s12, v252, 8
	v_lshlrev_b64 v[2:3], 21, v[34:35]
	v_readlane_b32 s13, v252, 9
	v_lshlrev_b32_e32 v4, 13, v4
	v_and_b32_e32 v34, 0x1c0000, v4
	v_lshl_add_u64 v[2:3], s[12:13], 0, v[2:3]
	v_lshlrev_b32_e32 v4, 7, v37
	v_lshl_add_u64 v[2:3], v[2:3], 0, v[34:35]
	v_and_b32_e32 v34, 0xf80, v4
	v_readlane_b32 s14, v252, 10
	v_readlane_b32 s15, v252, 11
	v_lshl_add_u64 v[2:3], v[2:3], 0, v[34:35]

; #define LAS __attribute__((address_space(3)))
; __device__ __forceinline__ int opaque_tid() { int t = threadIdx.x; asm volatile("" : "+v"(t)); return t; }
;     const int tid = opaque_tid(), lane = tid & 63, wave = tid >> 6;
;     LAS float* scr = (LAS float*)(lds + 49152) + wave * (64 * 33);
;     const int gw = ((int)blockIdx.x - blk0) * NWAVES + wave, ngw = nblk * NWAVES;
;     constexpr int I_L = 16 * 104 + 16 * 32 + 16 * 16 * 32 + 16 * 8 * 32;
;     if ((int)blockIdx.x < blk0 || (int)blockIdx.x >= blk0 + nblk) return;
;     float tv[32];
;     const int I_E = it_hi < I_L ? it_hi : I_L;
;     int it = it_lo + gw;
; __device__ __forceinline__ void pj_mfma(const Args& a, LAS unsigned char* lds, int layer) {
;     ...
;     if (layer + 1 < NL) { __syncthreads(); constexpr int I_SPLIT = 10240;
;         const int half = gridDim.x / 2; const bool upper = (int)blockIdx.x >= half;
;         p0_prep(a, lds, layer + 1, upper ? half : 0, upper ? (int)gridDim.x - half : half, upper ? 0 : I_SPLIT, upper ? I_SPLIT : (1 << 30)); }
.LBB0_345:
	s_or_b64 exec, exec, s[6:7]
	s_branch .LBB0_346
.Lpj_l1_prep:
	s_lshr_b32 s4, s77, 1
	s_sub_i32 s5, s77, s4
	s_cmp_ge_u32 s61, s4
	s_cselect_b64 s[6:7], -1, 0
	s_sub_i32 s8, s61, s4
	s_lshl_b32 s8, s8, 3
	s_addk_i32 s8, 0x1a80
	s_lshl_b32 s5, s5, 3
	s_movk_i32 s9, 0x2880
	s_nop 0
	v_writelane_b32 v252, s9, 36
	v_writelane_b32 v252, s5, 37
	v_writelane_b32 v252, s6, 38
	v_writelane_b32 v252, s7, 39
	v_writelane_b32 v252, s8, 40
	s_branch .Lprep_go
